# v32 + gate/up epilogue: the +1 of (clamp(up)+1) folded into the up bias (clamp bounds -6/8), 28 fewer packed adds per wave in the VALU-bound epilogue
# speedup vs baseline: 1.0093x; 1.0093x over previous
.LBB0_252:
	s_nop 15
	s_nop 15
	v_ashrrev_i32_e32 v23, 31, v22
	s_ashr_i32 s67, s66, 31
	s_add_u32 s100, s50, s66
	s_addc_u32 s101, s51, s67
	s_add_u32 s100, s100, s52
	s_addc_u32 s101, s101, s53
	v_lshlrev_b64 v[250:251], 10, v[22:23]
	v_lshl_add_u64 v[250:251], v[250:251], 0, s[100:101]
	v_lshl_add_u64 v[250:251], v[250:251], 0, v[166:167]
	s_mov_b64 s[26:27], -1
	s_and_b64 vcc, exec, s[38:39]
	s_waitcnt vmcnt(0)
	s_waitcnt lgkmcnt(0)
	v_mov_b32_e32 v230, 0xc0c00000
	v_mov_b32_e32 v231, 0x41000000
	v_pk_add_f32 v[6:7], v[6:7], 1.0 op_sel_hi:[1,0]
	v_pk_add_f32 v[8:9], v[8:9], 1.0 op_sel_hi:[1,0]
	v_pk_add_f32 v[14:15], v[14:15], 1.0 op_sel_hi:[1,0]
	v_pk_add_f32 v[16:17], v[16:17], 1.0 op_sel_hi:[1,0]
	v_pk_fma_f32 v[26:27], v[154:155], s[24:25], v[2:3] op_sel_hi:[1,0,1]
	v_pk_fma_f32 v[18:19], v[160:161], s[24:25], v[12:13] op_sel_hi:[1,0,1]
	v_pk_fma_f32 v[20:21], v[158:159], s[24:25], v[10:11] op_sel_hi:[1,0,1]
	v_min_f32_e32 v18, 0x40e00000, v18
	v_min_f32_e32 v20, 0x40e00000, v20
	v_min_f32_e32 v21, 0x40e00000, v21
	v_pk_fma_f32 v[30:31], v[150:151], s[24:25], v[6:7] op_sel_hi:[1,0,1]
	v_min_f32_e32 v19, 0x40e00000, v19
	v_med3_f32 v30, v30, v230, v231
	v_med3_f32 v31, v31, v230, v231
	v_pk_fma_f32 v[32:33], v[148:149], s[24:25], v[16:17] op_sel_hi:[1,0,1]
	v_pk_mul_f32 v[148:149], v[20:21], s[28:29] op_sel_hi:[1,0]
	v_pk_mul_f32 v[20:21], v[20:21], v[30:31]
	v_pk_mul_f32 v[30:31], v[18:19], s[28:29] op_sel_hi:[1,0]
	v_pk_fma_f32 v[24:25], v[152:153], s[24:25], v[8:9] op_sel_hi:[1,0,1]
	v_exp_f32_e32 v30, v30
	v_exp_f32_e32 v31, v31
	v_med3_f32 v24, v24, v230, v231
	v_med3_f32 v25, v25, v230, v231
	v_pk_add_f32 v[30:31], v[30:31], 1.0 op_sel_hi:[1,0]
	v_pk_mul_f32 v[18:19], v[18:19], v[24:25]
	v_rcp_f32_e32 v30, v30
	v_rcp_f32_e32 v31, v31
	v_pk_fma_f32 v[146:147], v[146:147], s[24:25], v[14:15] op_sel_hi:[1,0,1]
	v_pk_fma_f32 v[28:29], v[156:157], s[24:25], v[4:5] op_sel_hi:[1,0,1]
	v_exp_f32_e32 v148, v148
	v_pk_mul_f32 v[24:25], v[18:19], v[30:31]
	v_min_f32_e32 v18, 0x40e00000, v26
	v_min_f32_e32 v19, 0x40e00000, v27
	v_pk_mul_f32 v[30:31], v[18:19], s[28:29] op_sel_hi:[1,0]
	v_med3_f32 v26, v146, v230, v231
	v_exp_f32_e32 v30, v30
	v_exp_f32_e32 v31, v31
	v_med3_f32 v27, v147, v230, v231
	v_exp_f32_e32 v149, v149
	v_pk_add_f32 v[30:31], v[30:31], 1.0 op_sel_hi:[1,0]
	v_pk_mul_f32 v[18:19], v[18:19], v[26:27]
	v_rcp_f32_e32 v30, v30
	v_rcp_f32_e32 v31, v31
	v_pk_add_f32 v[148:149], v[148:149], 1.0 op_sel_hi:[1,0]
	v_pk_fma_f32 v[134:135], v[134:135], s[24:25], v[6:7] op_sel_hi:[1,0,1]
	v_rcp_f32_e32 v148, v148
	v_pk_mul_f32 v[26:27], v[18:19], v[30:31]
	v_min_f32_e32 v18, 0x40e00000, v28
	v_min_f32_e32 v19, 0x40e00000, v29
	v_pk_mul_f32 v[30:31], v[18:19], s[28:29] op_sel_hi:[1,0]
	v_rcp_f32_e32 v149, v149
	v_exp_f32_e32 v30, v30
	v_exp_f32_e32 v31, v31
	v_med3_f32 v28, v32, v230, v231
	v_med3_f32 v29, v33, v230, v231
	v_pk_add_f32 v[30:31], v[30:31], 1.0 op_sel_hi:[1,0]
	v_pk_mul_f32 v[18:19], v[18:19], v[28:29]
	v_rcp_f32_e32 v30, v30
	v_rcp_f32_e32 v31, v31
	v_pk_mul_f32 v[20:21], v[20:21], v[148:149]
	v_pk_fma_f32 v[32:33], v[136:137], s[24:25], v[8:9] op_sel_hi:[1,0,1]
	v_pk_fma_f32 v[142:143], v[142:143], s[24:25], v[10:11] op_sel_hi:[1,0,1]
	v_pk_mul_f32 v[28:29], v[18:19], v[30:31]
	v_cvt_pk_fp8_f32 v19, v26, v27
	v_cvt_pk_fp8_f32 v18, v20, v21
	v_pk_fma_f32 v[30:31], v[144:145], s[24:25], v[12:13] op_sel_hi:[1,0,1]
	v_pk_fma_f32 v[20:21], v[140:141], s[24:25], v[4:5] op_sel_hi:[1,0,1]
	v_cvt_pk_fp8_f32 v19, v28, v29 op_sel:[0,0,1]
	v_pk_fma_f32 v[28:29], v[130:131], s[24:25], v[14:15] op_sel_hi:[1,0,1]
	v_cvt_pk_fp8_f32 v18, v24, v25 op_sel:[0,0,1]
	v_pk_fma_f32 v[26:27], v[138:139], s[24:25], v[2:3] op_sel_hi:[1,0,1]
	v_pk_fma_f32 v[24:25], v[132:133], s[24:25], v[16:17] op_sel_hi:[1,0,1]
	v_med3_f32 v132, v134, v230, v231
	v_med3_f32 v133, v135, v230, v231
	v_med3_f32 v32, v32, v230, v231
	v_med3_f32 v33, v33, v230, v231
	v_med3_f32 v28, v28, v230, v231
	v_med3_f32 v29, v29, v230, v231
	v_min_f32_e32 v130, 0x40e00000, v142
	v_min_f32_e32 v131, 0x40e00000, v143
	v_min_f32_e32 v30, 0x40e00000, v30
	v_min_f32_e32 v31, 0x40e00000, v31
	v_min_f32_e32 v26, 0x40e00000, v26
	v_min_f32_e32 v27, 0x40e00000, v27
	v_min_f32_e32 v20, 0x40e00000, v20
	v_min_f32_e32 v21, 0x40e00000, v21
	v_pk_mul_f32 v[134:135], v[130:131], s[28:29] op_sel_hi:[1,0]
	v_pk_mul_f32 v[130:131], v[130:131], v[132:133]
	v_pk_mul_f32 v[132:133], v[30:31], s[28:29] op_sel_hi:[1,0]
	v_pk_mul_f32 v[30:31], v[30:31], v[32:33]
	v_pk_mul_f32 v[32:33], v[26:27], s[28:29] op_sel_hi:[1,0]
	v_pk_mul_f32 v[26:27], v[26:27], v[28:29]
	v_pk_mul_f32 v[28:29], v[20:21], s[28:29] op_sel_hi:[1,0]
	v_exp_f32_e32 v134, v134
	v_exp_f32_e32 v135, v135
	v_exp_f32_e32 v32, v32
	v_exp_f32_e32 v33, v33
	v_exp_f32_e32 v28, v28
	v_exp_f32_e32 v29, v29
	v_pk_add_f32 v[134:135], v[134:135], 1.0 op_sel_hi:[1,0]
	v_exp_f32_e32 v132, v132
	v_exp_f32_e32 v133, v133
	v_pk_add_f32 v[32:33], v[32:33], 1.0 op_sel_hi:[1,0]
	v_pk_add_f32 v[28:29], v[28:29], 1.0 op_sel_hi:[1,0]
	v_rcp_f32_e32 v134, v134
	v_rcp_f32_e32 v135, v135
	v_rcp_f32_e32 v32, v32
	v_rcp_f32_e32 v33, v33
	v_rcp_f32_e32 v28, v28
	v_rcp_f32_e32 v29, v29
	v_med3_f32 v24, v24, v230, v231
	v_med3_f32 v25, v25, v230, v231
	v_pk_add_f32 v[132:133], v[132:133], 1.0 op_sel_hi:[1,0]
	v_pk_mul_f32 v[20:21], v[20:21], v[24:25]
	v_pk_mul_f32 v[130:131], v[130:131], v[134:135]
	v_rcp_f32_e32 v132, v132
	v_rcp_f32_e32 v133, v133
	v_pk_mul_f32 v[26:27], v[26:27], v[32:33]
	v_pk_mul_f32 v[24:25], v[20:21], v[28:29]
	v_cvt_pk_fp8_f32 v20, v130, v131
	v_cvt_pk_fp8_f32 v21, v26, v27
	v_pk_mul_f32 v[30:31], v[30:31], v[132:133]
	v_pk_fma_f32 v[32:33], v[116:117], s[24:25], v[16:17] op_sel_hi:[1,0,1]
	v_cvt_pk_fp8_f32 v20, v30, v31 op_sel:[0,0,1]
	v_cvt_pk_fp8_f32 v21, v24, v25 op_sel:[0,0,1]
	v_permlane16_swap_b32_e32 v18, v20
	v_permlane16_swap_b32_e32 v19, v21
	v_pk_fma_f32 v[30:31], v[118:119], s[24:25], v[6:7] op_sel_hi:[1,0,1]
	global_store_dwordx4 v[250:251], v[18:21], off
	v_med3_f32 v30, v30, v230, v231
	v_med3_f32 v31, v31, v230, v231
	v_pk_fma_f32 v[18:19], v[128:129], s[24:25], v[12:13] op_sel_hi:[1,0,1]
	v_pk_fma_f32 v[20:21], v[126:127], s[24:25], v[10:11] op_sel_hi:[1,0,1]
	v_min_f32_e32 v20, 0x40e00000, v20
	v_min_f32_e32 v21, 0x40e00000, v21
	v_min_f32_e32 v18, 0x40e00000, v18
	v_min_f32_e32 v19, 0x40e00000, v19
	v_pk_mul_f32 v[116:117], v[20:21], s[28:29] op_sel_hi:[1,0]
	v_pk_mul_f32 v[20:21], v[20:21], v[30:31]
	v_pk_mul_f32 v[30:31], v[18:19], s[28:29] op_sel_hi:[1,0]
	v_pk_fma_f32 v[28:29], v[120:121], s[24:25], v[8:9] op_sel_hi:[1,0,1]
	v_exp_f32_e32 v30, v30
	v_exp_f32_e32 v31, v31
	v_med3_f32 v28, v28, v230, v231
	v_med3_f32 v29, v29, v230, v231
	v_pk_add_f32 v[30:31], v[30:31], 1.0 op_sel_hi:[1,0]
	v_pk_fma_f32 v[26:27], v[122:123], s[24:25], v[2:3] op_sel_hi:[1,0,1]
	v_rcp_f32_e32 v30, v30
	v_rcp_f32_e32 v31, v31
	v_pk_mul_f32 v[18:19], v[18:19], v[28:29]
	v_pk_fma_f32 v[114:115], v[114:115], s[24:25], v[14:15] op_sel_hi:[1,0,1]
	v_pk_fma_f32 v[24:25], v[124:125], s[24:25], v[4:5] op_sel_hi:[1,0,1]
	v_pk_mul_f32 v[28:29], v[18:19], v[30:31]
	v_min_f32_e32 v18, 0x40e00000, v26
	v_min_f32_e32 v19, 0x40e00000, v27
	v_pk_mul_f32 v[30:31], v[18:19], s[28:29] op_sel_hi:[1,0]
	v_med3_f32 v26, v114, v230, v231
	v_exp_f32_e32 v30, v30
	v_exp_f32_e32 v31, v31
	v_med3_f32 v27, v115, v230, v231
	v_exp_f32_e32 v116, v116
	v_pk_add_f32 v[30:31], v[30:31], 1.0 op_sel_hi:[1,0]
	v_pk_mul_f32 v[18:19], v[18:19], v[26:27]
	v_rcp_f32_e32 v30, v30
	v_rcp_f32_e32 v31, v31
	v_exp_f32_e32 v117, v117
	v_pk_fma_f32 v[98:99], v[98:99], s[24:25], v[14:15] op_sel_hi:[1,0,1]
	v_pk_fma_f32 v[100:101], v[100:101], s[24:25], v[16:17] op_sel_hi:[1,0,1]
	v_pk_mul_f32 v[26:27], v[18:19], v[30:31]
	v_min_f32_e32 v18, 0x40e00000, v24
	v_min_f32_e32 v19, 0x40e00000, v25
	v_pk_mul_f32 v[30:31], v[18:19], s[28:29] op_sel_hi:[1,0]
	v_med3_f32 v24, v32, v230, v231
	v_exp_f32_e32 v30, v30
	v_exp_f32_e32 v31, v31
	v_med3_f32 v25, v33, v230, v231
	v_pk_add_f32 v[116:117], v[116:117], 1.0 op_sel_hi:[1,0]
	v_pk_add_f32 v[30:31], v[30:31], 1.0 op_sel_hi:[1,0]
	v_pk_mul_f32 v[18:19], v[18:19], v[24:25]
	v_rcp_f32_e32 v30, v30
	v_rcp_f32_e32 v31, v31
	v_rcp_f32_e32 v116, v116
	v_rcp_f32_e32 v117, v117
	v_pk_fma_f32 v[32:33], v[102:103], s[24:25], v[6:7] op_sel_hi:[1,0,1]
	v_pk_mul_f32 v[24:25], v[18:19], v[30:31]
	v_cvt_pk_fp8_f32 v19, v26, v27
	v_pk_mul_f32 v[20:21], v[20:21], v[116:117]
	v_cvt_pk_fp8_f32 v18, v20, v21
	v_cvt_pk_fp8_f32 v19, v24, v25 op_sel:[0,0,1]
	v_pk_fma_f32 v[20:21], v[112:113], s[24:25], v[12:13] op_sel_hi:[1,0,1]
	v_pk_fma_f32 v[24:25], v[110:111], s[24:25], v[10:11] op_sel_hi:[1,0,1]
	v_med3_f32 v32, v32, v230, v231
	v_med3_f32 v33, v33, v230, v231
	v_min_f32_e32 v24, 0x40e00000, v24
	v_min_f32_e32 v25, 0x40e00000, v25
	v_min_f32_e32 v20, 0x40e00000, v20
	v_min_f32_e32 v21, 0x40e00000, v21
	v_pk_mul_f32 v[102:103], v[24:25], s[28:29] op_sel_hi:[1,0]
	v_pk_mul_f32 v[24:25], v[24:25], v[32:33]
	v_pk_mul_f32 v[32:33], v[20:21], s[28:29] op_sel_hi:[1,0]
	v_pk_fma_f32 v[30:31], v[104:105], s[24:25], v[8:9] op_sel_hi:[1,0,1]
	v_exp_f32_e32 v32, v32
	v_exp_f32_e32 v33, v33
	v_med3_f32 v30, v30, v230, v231
	v_med3_f32 v31, v31, v230, v231
	v_pk_add_f32 v[32:33], v[32:33], 1.0 op_sel_hi:[1,0]
	v_cvt_pk_fp8_f32 v18, v28, v29 op_sel:[0,0,1]
	v_rcp_f32_e32 v32, v32
	v_rcp_f32_e32 v33, v33
	v_pk_fma_f32 v[28:29], v[106:107], s[24:25], v[2:3] op_sel_hi:[1,0,1]
	v_pk_mul_f32 v[20:21], v[20:21], v[30:31]
	v_pk_fma_f32 v[26:27], v[108:109], s[24:25], v[4:5] op_sel_hi:[1,0,1]
	v_pk_mul_f32 v[30:31], v[20:21], v[32:33]
	v_min_f32_e32 v20, 0x40e00000, v28
	v_min_f32_e32 v21, 0x40e00000, v29
	v_pk_mul_f32 v[32:33], v[20:21], s[28:29] op_sel_hi:[1,0]
	v_med3_f32 v28, v98, v230, v231
	v_exp_f32_e32 v32, v32
	v_exp_f32_e32 v33, v33
	v_med3_f32 v29, v99, v230, v231
	v_exp_f32_e32 v102, v102
	v_pk_add_f32 v[32:33], v[32:33], 1.0 op_sel_hi:[1,0]
	v_pk_mul_f32 v[20:21], v[20:21], v[28:29]
	v_rcp_f32_e32 v32, v32
	v_rcp_f32_e32 v33, v33
	v_exp_f32_e32 v103, v103
	v_pk_fma_f32 v[82:83], v[82:83], s[24:25], v[14:15] op_sel_hi:[1,0,1]
	v_pk_fma_f32 v[84:85], v[84:85], s[24:25], v[16:17] op_sel_hi:[1,0,1]
	v_pk_mul_f32 v[28:29], v[20:21], v[32:33]
	v_min_f32_e32 v20, 0x40e00000, v26
	v_min_f32_e32 v21, 0x40e00000, v27
	v_pk_mul_f32 v[32:33], v[20:21], s[28:29] op_sel_hi:[1,0]
	v_pk_add_f32 v[102:103], v[102:103], 1.0 op_sel_hi:[1,0]
	v_exp_f32_e32 v32, v32
	v_exp_f32_e32 v33, v33
	v_rcp_f32_e32 v102, v102
	v_rcp_f32_e32 v103, v103
	v_med3_f32 v26, v100, v230, v231
	v_pk_add_f32 v[32:33], v[32:33], 1.0 op_sel_hi:[1,0]
	v_med3_f32 v27, v101, v230, v231
	v_rcp_f32_e32 v32, v32
	v_rcp_f32_e32 v33, v33
	v_pk_mul_f32 v[24:25], v[24:25], v[102:103]
	v_pk_mul_f32 v[20:21], v[20:21], v[26:27]
	s_nop 0
	v_pk_mul_f32 v[26:27], v[20:21], v[32:33]
	v_cvt_pk_fp8_f32 v20, v24, v25
	v_cvt_pk_fp8_f32 v21, v28, v29
	v_cvt_pk_fp8_f32 v20, v30, v31 op_sel:[0,0,1]
	v_cvt_pk_fp8_f32 v21, v26, v27 op_sel:[0,0,1]
	v_permlane16_swap_b32_e32 v18, v20
	v_permlane16_swap_b32_e32 v19, v21
	s_mov_b64 s[100:101], 0x8000
	v_lshl_add_u64 v[24:25], v[250:251], 0, s[100:101]
	v_pk_fma_f32 v[32:33], v[86:87], s[24:25], v[6:7] op_sel_hi:[1,0,1]
	global_store_dwordx4 v[24:25], v[18:21], off
	v_med3_f32 v32, v32, v230, v231
	v_med3_f32 v33, v33, v230, v231
	v_pk_fma_f32 v[18:19], v[96:97], s[24:25], v[12:13] op_sel_hi:[1,0,1]
	v_pk_fma_f32 v[20:21], v[94:95], s[24:25], v[10:11] op_sel_hi:[1,0,1]
	v_min_f32_e32 v20, 0x40e00000, v20
	v_min_f32_e32 v21, 0x40e00000, v21
	v_min_f32_e32 v18, 0x40e00000, v18
	v_min_f32_e32 v19, 0x40e00000, v19
	v_pk_mul_f32 v[86:87], v[20:21], s[28:29] op_sel_hi:[1,0]
	v_pk_mul_f32 v[20:21], v[20:21], v[32:33]
	v_pk_mul_f32 v[32:33], v[18:19], s[28:29] op_sel_hi:[1,0]
	v_pk_fma_f32 v[30:31], v[88:89], s[24:25], v[8:9] op_sel_hi:[1,0,1]
	v_exp_f32_e32 v32, v32
	v_exp_f32_e32 v33, v33
	v_med3_f32 v30, v30, v230, v231
	v_med3_f32 v31, v31, v230, v231
	v_pk_add_f32 v[32:33], v[32:33], 1.0 op_sel_hi:[1,0]
	v_pk_fma_f32 v[28:29], v[90:91], s[24:25], v[2:3] op_sel_hi:[1,0,1]
	v_rcp_f32_e32 v32, v32
	v_rcp_f32_e32 v33, v33
	v_pk_mul_f32 v[18:19], v[18:19], v[30:31]
	v_pk_fma_f32 v[26:27], v[92:93], s[24:25], v[4:5] op_sel_hi:[1,0,1]
	v_exp_f32_e32 v86, v86
	v_pk_mul_f32 v[30:31], v[18:19], v[32:33]
	v_min_f32_e32 v18, 0x40e00000, v28
	v_min_f32_e32 v19, 0x40e00000, v29
	v_pk_mul_f32 v[32:33], v[18:19], s[28:29] op_sel_hi:[1,0]
	v_med3_f32 v28, v82, v230, v231
	v_exp_f32_e32 v32, v32
	v_exp_f32_e32 v33, v33
	v_med3_f32 v29, v83, v230, v231
	v_exp_f32_e32 v87, v87
	v_pk_add_f32 v[32:33], v[32:33], 1.0 op_sel_hi:[1,0]
	v_pk_mul_f32 v[18:19], v[18:19], v[28:29]
	v_rcp_f32_e32 v32, v32
	v_rcp_f32_e32 v33, v33
	v_pk_add_f32 v[86:87], v[86:87], 1.0 op_sel_hi:[1,0]
	v_rcp_f32_e32 v86, v86
	v_pk_mul_f32 v[28:29], v[18:19], v[32:33]
	v_min_f32_e32 v18, 0x40e00000, v26
	v_min_f32_e32 v19, 0x40e00000, v27
	v_pk_mul_f32 v[32:33], v[18:19], s[28:29] op_sel_hi:[1,0]
	v_rcp_f32_e32 v87, v87
	v_exp_f32_e32 v32, v32
	v_exp_f32_e32 v33, v33
	v_med3_f32 v26, v84, v230, v231
	v_med3_f32 v27, v85, v230, v231
	v_pk_add_f32 v[32:33], v[32:33], 1.0 op_sel_hi:[1,0]
	v_pk_mul_f32 v[18:19], v[18:19], v[26:27]
	v_rcp_f32_e32 v32, v32
	v_rcp_f32_e32 v33, v33
	v_pk_mul_f32 v[20:21], v[20:21], v[86:87]
	v_pk_mul_f32 v[26:27], v[18:19], v[32:33]
	v_cvt_pk_fp8_f32 v18, v20, v21
	v_cvt_pk_fp8_f32 v19, v28, v29
	v_pk_fma_f32 v[20:21], v[72:73], s[24:25], v[12:13] op_sel_hi:[1,0,1]
	v_cvt_pk_fp8_f32 v18, v30, v31 op_sel:[0,0,1]
	v_pk_fma_f32 v[30:31], v[66:67], s[24:25], v[2:3] op_sel_hi:[1,0,1]
	v_pk_fma_f32 v[66:67], v[78:79], s[24:25], v[6:7] op_sel_hi:[1,0,1]
	v_cvt_pk_fp8_f32 v19, v26, v27 op_sel:[0,0,1]
	v_pk_fma_f32 v[26:27], v[70:71], s[24:25], v[10:11] op_sel_hi:[1,0,1]
	v_med3_f32 v66, v66, v230, v231
	v_med3_f32 v67, v67, v230, v231
	v_min_f32_e32 v26, 0x40e00000, v26
	v_min_f32_e32 v27, 0x40e00000, v27
	v_min_f32_e32 v20, 0x40e00000, v20
	v_min_f32_e32 v21, 0x40e00000, v21
	v_pk_mul_f32 v[72:73], v[26:27], s[28:29] op_sel_hi:[1,0]
	v_pk_mul_f32 v[26:27], v[26:27], v[66:67]
	v_pk_mul_f32 v[66:67], v[20:21], s[28:29] op_sel_hi:[1,0]
	v_pk_fma_f32 v[32:33], v[80:81], s[24:25], v[8:9] op_sel_hi:[1,0,1]
	v_exp_f32_e32 v66, v66
	v_exp_f32_e32 v67, v67
	v_med3_f32 v32, v32, v230, v231
	v_med3_f32 v33, v33, v230, v231
	v_pk_add_f32 v[66:67], v[66:67], 1.0 op_sel_hi:[1,0]
	v_pk_mul_f32 v[20:21], v[20:21], v[32:33]
	v_rcp_f32_e32 v66, v66
	v_rcp_f32_e32 v67, v67
	v_pk_fma_f32 v[70:71], v[74:75], s[24:25], v[14:15] op_sel_hi:[1,0,1]
	v_pk_fma_f32 v[28:29], v[68:69], s[24:25], v[4:5] op_sel_hi:[1,0,1]
	v_exp_f32_e32 v72, v72
	v_pk_mul_f32 v[32:33], v[20:21], v[66:67]
	v_min_f32_e32 v20, 0x40e00000, v30
	v_min_f32_e32 v21, 0x40e00000, v31
	v_pk_mul_f32 v[66:67], v[20:21], s[28:29] op_sel_hi:[1,0]
	v_med3_f32 v30, v70, v230, v231
	v_exp_f32_e32 v66, v66
	v_exp_f32_e32 v67, v67
	v_med3_f32 v31, v71, v230, v231
	v_exp_f32_e32 v73, v73
	v_pk_add_f32 v[66:67], v[66:67], 1.0 op_sel_hi:[1,0]
	v_pk_mul_f32 v[20:21], v[20:21], v[30:31]
	v_rcp_f32_e32 v66, v66
	v_rcp_f32_e32 v67, v67
	v_pk_add_f32 v[72:73], v[72:73], 1.0 op_sel_hi:[1,0]
	v_pk_fma_f32 v[68:69], v[76:77], s[24:25], v[16:17] op_sel_hi:[1,0,1]
	v_rcp_f32_e32 v72, v72
	v_pk_mul_f32 v[30:31], v[20:21], v[66:67]
	v_min_f32_e32 v20, 0x40e00000, v28
	v_min_f32_e32 v21, 0x40e00000, v29
	v_pk_mul_f32 v[66:67], v[20:21], s[28:29] op_sel_hi:[1,0]
	v_rcp_f32_e32 v73, v73
	v_exp_f32_e32 v66, v66
	v_exp_f32_e32 v67, v67
	v_med3_f32 v28, v68, v230, v231
	v_med3_f32 v29, v69, v230, v231
	v_pk_add_f32 v[66:67], v[66:67], 1.0 op_sel_hi:[1,0]
	v_pk_mul_f32 v[20:21], v[20:21], v[28:29]
	v_rcp_f32_e32 v66, v66
	v_rcp_f32_e32 v67, v67
	v_pk_mul_f32 v[26:27], v[26:27], v[72:73]
	v_pk_mul_f32 v[28:29], v[20:21], v[66:67]
	v_cvt_pk_fp8_f32 v20, v26, v27
	v_cvt_pk_fp8_f32 v21, v30, v31
	s_mov_b64 s[100:101], 0x20000
	v_lshl_add_u64 v[24:25], v[250:251], 0, s[100:101]
	v_cvt_pk_fp8_f32 v20, v32, v33 op_sel:[0,0,1]
	v_cvt_pk_fp8_f32 v21, v28, v29 op_sel:[0,0,1]
	v_pk_fma_f32 v[30:31], v[62:63], s[24:25], v[6:7] op_sel_hi:[1,0,1]
	v_pk_fma_f32 v[28:29], v[64:65], s[24:25], v[8:9] op_sel_hi:[1,0,1]
	v_permlane16_swap_b32_e32 v18, v20
	v_permlane16_swap_b32_e32 v19, v21
	global_store_dwordx4 v[24:25], v[18:21], off
	v_med3_f32 v30, v30, v230, v231
	v_med3_f32 v31, v31, v230, v231
	v_pk_fma_f32 v[18:19], v[56:57], s[24:25], v[12:13] op_sel_hi:[1,0,1]
	v_pk_fma_f32 v[20:21], v[54:55], s[24:25], v[10:11] op_sel_hi:[1,0,1]
	v_min_f32_e32 v20, 0x40e00000, v20
	v_min_f32_e32 v21, 0x40e00000, v21
	v_min_f32_e32 v18, 0x40e00000, v18
	v_min_f32_e32 v19, 0x40e00000, v19
	v_pk_fma_f32 v[24:25], v[52:53], s[24:25], v[4:5] op_sel_hi:[1,0,1]
	v_pk_mul_f32 v[52:53], v[20:21], s[28:29] op_sel_hi:[1,0]
	v_pk_mul_f32 v[20:21], v[20:21], v[30:31]
	v_pk_mul_f32 v[30:31], v[18:19], s[28:29] op_sel_hi:[1,0]
	v_med3_f32 v28, v28, v230, v231
	v_exp_f32_e32 v30, v30
	v_exp_f32_e32 v31, v31
	v_med3_f32 v29, v29, v230, v231
	v_pk_fma_f32 v[26:27], v[50:51], s[24:25], v[2:3] op_sel_hi:[1,0,1]
	v_pk_add_f32 v[30:31], v[30:31], 1.0 op_sel_hi:[1,0]
	v_pk_mul_f32 v[18:19], v[18:19], v[28:29]
	v_rcp_f32_e32 v30, v30
	v_rcp_f32_e32 v31, v31
	v_pk_fma_f32 v[50:51], v[58:59], s[24:25], v[14:15] op_sel_hi:[1,0,1]
	v_exp_f32_e32 v52, v52
	v_exp_f32_e32 v53, v53
	v_pk_mul_f32 v[28:29], v[18:19], v[30:31]
	v_min_f32_e32 v18, 0x40e00000, v26
	v_min_f32_e32 v19, 0x40e00000, v27
	v_pk_mul_f32 v[30:31], v[18:19], s[28:29] op_sel_hi:[1,0]
	v_med3_f32 v26, v50, v230, v231
	v_exp_f32_e32 v30, v30
	v_exp_f32_e32 v31, v31
	v_med3_f32 v27, v51, v230, v231
	v_pk_add_f32 v[52:53], v[52:53], 1.0 op_sel_hi:[1,0]
	v_pk_add_f32 v[30:31], v[30:31], 1.0 op_sel_hi:[1,0]
	v_pk_mul_f32 v[18:19], v[18:19], v[26:27]
	v_rcp_f32_e32 v30, v30
	v_rcp_f32_e32 v31, v31
	v_pk_fma_f32 v[32:33], v[60:61], s[24:25], v[16:17] op_sel_hi:[1,0,1]
	v_rcp_f32_e32 v52, v52
	v_rcp_f32_e32 v53, v53
	v_pk_mul_f32 v[26:27], v[18:19], v[30:31]
	v_min_f32_e32 v18, 0x40e00000, v24
	v_min_f32_e32 v19, 0x40e00000, v25
	v_pk_mul_f32 v[30:31], v[18:19], s[28:29] op_sel_hi:[1,0]
	v_med3_f32 v24, v32, v230, v231
	v_exp_f32_e32 v30, v30
	v_exp_f32_e32 v31, v31
	v_med3_f32 v25, v33, v230, v231
	v_pk_fma_f32 v[6:7], v[46:47], s[24:25], v[6:7] op_sel_hi:[1,0,1]
	v_pk_add_f32 v[30:31], v[30:31], 1.0 op_sel_hi:[1,0]
	v_pk_mul_f32 v[18:19], v[18:19], v[24:25]
	v_rcp_f32_e32 v30, v30
	v_rcp_f32_e32 v31, v31
	v_pk_fma_f32 v[10:11], v[38:39], s[24:25], v[10:11] op_sel_hi:[1,0,1]
	v_med3_f32 v6, v6, v230, v231
	v_med3_f32 v7, v7, v230, v231
	v_pk_mul_f32 v[20:21], v[20:21], v[52:53]
	v_pk_mul_f32 v[24:25], v[18:19], v[30:31]
	v_pk_fma_f32 v[12:13], v[40:41], s[24:25], v[12:13] op_sel_hi:[1,0,1]
	v_min_f32_e32 v10, 0x40e00000, v10
	v_min_f32_e32 v11, 0x40e00000, v11
	v_cvt_pk_fp8_f32 v18, v20, v21
	v_pk_mul_f32 v[20:21], v[10:11], s[28:29] op_sel_hi:[1,0]
	v_pk_mul_f32 v[6:7], v[10:11], v[6:7]
	v_min_f32_e32 v10, 0x40e00000, v12
	v_min_f32_e32 v11, 0x40e00000, v13
	v_pk_mul_f32 v[12:13], v[10:11], s[28:29] op_sel_hi:[1,0]
	v_pk_fma_f32 v[8:9], v[48:49], s[24:25], v[8:9] op_sel_hi:[1,0,1]
	v_exp_f32_e32 v12, v12
	v_exp_f32_e32 v13, v13
	v_med3_f32 v8, v8, v230, v231
	v_med3_f32 v9, v9, v230, v231
	v_pk_fma_f32 v[2:3], v[34:35], s[24:25], v[2:3] op_sel_hi:[1,0,1]
	v_pk_add_f32 v[12:13], v[12:13], 1.0 op_sel_hi:[1,0]
	v_rcp_f32_e32 v12, v12
	v_rcp_f32_e32 v13, v13
	v_pk_mul_f32 v[8:9], v[10:11], v[8:9]
	v_min_f32_e32 v2, 0x40e00000, v2
	v_min_f32_e32 v3, 0x40e00000, v3
	v_pk_mul_f32 v[8:9], v[8:9], v[12:13]
	v_pk_mul_f32 v[12:13], v[2:3], s[28:29] op_sel_hi:[1,0]
	v_pk_fma_f32 v[14:15], v[42:43], s[24:25], v[14:15] op_sel_hi:[1,0,1]
	v_exp_f32_e32 v12, v12
	v_exp_f32_e32 v13, v13
	v_exp_f32_e32 v20, v20
	v_exp_f32_e32 v21, v21
	v_med3_f32 v10, v14, v230, v231
	v_pk_add_f32 v[12:13], v[12:13], 1.0 op_sel_hi:[1,0]
	v_med3_f32 v11, v15, v230, v231
	v_rcp_f32_e32 v12, v12
	v_rcp_f32_e32 v13, v13
	v_pk_fma_f32 v[4:5], v[36:37], s[24:25], v[4:5] op_sel_hi:[1,0,1]
	v_min_f32_e32 v4, 0x40e00000, v4
	v_pk_mul_f32 v[2:3], v[2:3], v[10:11]
	v_min_f32_e32 v5, 0x40e00000, v5
	v_pk_mul_f32 v[2:3], v[2:3], v[12:13]
	v_pk_mul_f32 v[12:13], v[4:5], s[28:29] op_sel_hi:[1,0]
	v_pk_add_f32 v[20:21], v[20:21], 1.0 op_sel_hi:[1,0]
	v_exp_f32_e32 v12, v12
	v_exp_f32_e32 v13, v13
	v_rcp_f32_e32 v20, v20
	v_rcp_f32_e32 v21, v21
	v_pk_add_f32 v[12:13], v[12:13], 1.0 op_sel_hi:[1,0]
	v_pk_fma_f32 v[16:17], v[44:45], s[24:25], v[16:17] op_sel_hi:[1,0,1]
	v_pk_mul_f32 v[6:7], v[6:7], v[20:21]
	v_rcp_f32_e32 v12, v12
	v_rcp_f32_e32 v13, v13
	v_cvt_pk_fp8_f32 v19, v26, v27
	v_med3_f32 v10, v16, v230, v231
	v_med3_f32 v11, v17, v230, v231
	v_cvt_pk_fp8_f32 v20, v6, v7
	v_cvt_pk_fp8_f32 v21, v2, v3
	v_pk_mul_f32 v[4:5], v[4:5], v[10:11]
	v_pk_mul_f32 v[4:5], v[4:5], v[12:13]
	v_cvt_pk_fp8_f32 v18, v28, v29 op_sel:[0,0,1]
	v_cvt_pk_fp8_f32 v19, v24, v25 op_sel:[0,0,1]
	v_cvt_pk_fp8_f32 v20, v8, v9 op_sel:[0,0,1]
	v_cvt_pk_fp8_f32 v21, v4, v5 op_sel:[0,0,1]
	v_permlane16_swap_b32_e32 v18, v20
	v_permlane16_swap_b32_e32 v19, v21
	s_mov_b64 s[100:101], 0x28000
	v_lshl_add_u64 v[2:3], v[250:251], 0, s[100:101]
	global_store_dwordx4 v[2:3], v[18:21], off
	s_cbranch_vccnz .LBB0_237
	s_andn2_b64 vcc, exec, s[42:43]
	s_cbranch_vccnz .LBB0_236
	s_barrier
	s_branch .LBB0_236
